# gemm: one static s_setprio 1 for the younger wave half (waves 4-7) across the main loop, on top of the balanced read split
# baseline (speedup 1.0000x reference)
_Z8gemm_qkvPKDF16_S0_PKfPDF16_S3_S3_Pj:
	v_readfirstlane_b32 s13, v0
	s_lshr_b32 s8, s13, 6
	v_bfe_u32 v2, v0, 3, 3
	s_load_dwordx4 s[4:7], s[0:1], 0x0
	v_lshl_or_b32 v6, s8, 3, v2
	v_lshrrev_b32_e32 v2, 1, v6
	s_mul_i32 s16, s3, 0xc0
	v_xor_b32_e32 v4, v2, v0
	v_add_u32_e32 v2, s16, v6
	v_ashrrev_i32_e32 v3, 31, v2
	s_bfe_u32 s15, s13, 0x20006
	v_lshlrev_b64 v[2:3], 11, v[2:3]
	v_lshlrev_b32_e32 v4, 4, v4
	s_mul_i32 s10, s2, 0xc0
	s_mul_i32 s2, s15, 48
	s_waitcnt lgkmcnt(0)
	v_lshl_add_u64 v[2:3], s[4:5], 0, v[2:3]
	v_and_b32_e32 v4, 0x70, v4
	v_mov_b32_e32 v5, 0
	s_add_i32 s17, s2, s10
	v_lshl_add_u64 v[218:219], v[2:3], 0, v[4:5]
	v_add_u32_e32 v2, s10, v6
	s_lshl_b32 s8, s8, 10
	v_ashrrev_i32_e32 v3, 31, v2
	s_cmp_lg_u32 0x400, -1
	v_lshlrev_b64 v[2:3], 11, v[2:3]
	s_cselect_b32 s4, 0x400, 0
	v_lshl_add_u64 v[2:3], s[6:7], 0, v[2:3]
	s_add_i32 s11, s8, s4
	s_mov_b32 s4, m0
	s_mov_b32 m0, s11
	s_nop 0
	global_load_lds_dwordx4 v[218:219], off
	s_mov_b32 m0, s4
	v_lshl_add_u64 v[220:221], v[2:3], 0, v[4:5]
	s_add_i32 s4, s11, 0x6000
	s_mov_b32 s5, m0
	s_mov_b32 m0, s4
	s_nop 0
	global_load_lds_dwordx4 v[220:221], off
	s_mov_b32 m0, s5
	s_mov_b64 s[4:5], 0x20000
	v_lshl_add_u64 v[222:223], v[218:219], 0, s[4:5]
	s_add_i32 s9, s11, 0x2000
	s_mov_b32 s6, m0
	s_mov_b32 m0, s9
	s_nop 0
	global_load_lds_dwordx4 v[222:223], off
	s_mov_b32 m0, s6
	v_lshl_add_u64 v[224:225], v[220:221], 0, s[4:5]
	s_add_i32 s4, s11, 0x8000
	s_mov_b32 s5, m0
	s_mov_b32 m0, s4
	s_nop 0
	global_load_lds_dwordx4 v[224:225], off
	s_mov_b32 m0, s5
	s_mov_b64 s[4:5], 0x40000
	v_lshl_add_u64 v[226:227], v[218:219], 0, s[4:5]
	s_add_i32 s12, s11, 0x4000
	s_mov_b32 s6, m0
	s_mov_b32 m0, s12
	s_nop 0
	global_load_lds_dwordx4 v[226:227], off
	s_mov_b32 m0, s6
	v_lshl_add_u64 v[228:229], v[220:221], 0, s[4:5]
	s_add_i32 s4, s11, 0xa000
	s_mov_b32 s5, m0
	s_mov_b32 m0, s4
	s_nop 0
	global_load_lds_dwordx4 v[228:229], off
	s_mov_b32 m0, s5
	s_cmpk_gt_i32 s17, 0x7d0
	s_cselect_b64 s[4:5], -1, 0
	s_lshr_b32 s14, s13, 8
	s_mul_i32 s6, s14, 0x3000
	s_add_i32 s13, s6, 0x400
	s_mov_b64 s[6:7], 0x80
	s_add_i32 s18, s11, 0xc000
	v_lshl_add_u64 v[2:3], v[218:219], 0, s[6:7]
	s_mov_b32 s30, m0
	s_mov_b32 m0, s18
	s_nop 0
	global_load_lds_dwordx4 v[2:3], off
	s_mov_b32 m0, s30
	s_add_i32 s19, s11, 0x12000
	v_lshl_add_u64 v[2:3], v[220:221], 0, s[6:7]
	s_mov_b32 s6, m0
	s_mov_b32 m0, s19
	s_nop 0
	global_load_lds_dwordx4 v[2:3], off
	s_mov_b32 m0, s6
	s_mov_b64 s[6:7], 0x20080
	s_add_i32 s20, s11, 0xe000
	v_lshl_add_u64 v[2:3], v[218:219], 0, s[6:7]
	s_mov_b32 s18, m0
	s_mov_b32 m0, s20
	s_nop 0
	global_load_lds_dwordx4 v[2:3], off
	s_mov_b32 m0, s18
	s_add_i32 s21, s11, 0x14000
	v_lshl_add_u64 v[2:3], v[220:221], 0, s[6:7]
	s_mov_b32 s6, m0
	s_mov_b32 m0, s21
	s_nop 0
	global_load_lds_dwordx4 v[2:3], off
	s_mov_b32 m0, s6
	s_mov_b64 s[6:7], 0x40080
	v_lshl_add_u64 v[2:3], v[218:219], 0, s[6:7]
	s_add_i32 s22, s11, 0x10000
	s_mov_b32 s18, m0
	s_mov_b32 m0, s22
	s_nop 0
	global_load_lds_dwordx4 v[2:3], off
	s_mov_b32 m0, s18
	v_lshl_add_u64 v[2:3], v[220:221], 0, s[6:7]
	v_and_b32_e32 v1, 15, v0
	v_bfe_u32 v231, v0, 4, 2
	s_add_i32 s23, s11, 0x16000
	s_mov_b32 s6, m0
	s_mov_b32 m0, s23
	s_nop 0
	global_load_lds_dwordx4 v[2:3], off
	s_mov_b32 m0, s6
	v_lshrrev_b32_e32 v3, 1, v0
	v_lshlrev_b32_e32 v2, 7, v1
	v_bfe_u32 v4, v0, 1, 3
	v_bitop3_b32 v3, v231, v3, 7 bitop3:0x78
	v_lshl_or_b32 v238, v3, 4, v2
	v_bitop3_b32 v3, v231, v4, 4 bitop3:0x36
	v_lshl_or_b32 v240, v3, 4, v2
	s_mulk_i32 s15, 0x1800
	s_addk_i32 s15, 0x6400
	v_add_u32_e32 v158, s13, v238
	v_add_u32_e32 v160, s13, v240
	v_add_u32_e32 v162, s15, v238
	v_add_u32_e32 v164, s15, v240
	s_add_u32 m0, s11, 0x17f00
	s_nop 0
	global_load_lds_dwordx4 v[218:219], off offset:256
	s_add_u32 m0, s11, 0x19f00
	s_nop 0
	global_load_lds_dwordx4 v[222:223], off offset:256
	s_add_u32 m0, s11, 0x1bf00
	s_nop 0
	global_load_lds_dwordx4 v[226:227], off offset:256
	s_load_dwordx2 s[24:25], s[0:1], 0x10
	s_mov_b32 s20, 0x180
	s_mov_b32 s21, 0
	v_lshl_add_u64 v[218:219], v[218:219], 0, s[20:21]
	v_lshl_add_u64 v[222:223], v[222:223], 0, s[20:21]
	v_lshl_add_u64 v[226:227], v[226:227], 0, s[20:21]
	v_lshl_add_u64 v[220:221], v[220:221], 0, s[20:21]
	v_lshl_add_u64 v[224:225], v[224:225], 0, s[20:21]
	v_lshl_add_u64 v[228:229], v[228:229], 0, s[20:21]
	v_add_u32_e32 v159, 0x18000, v158
	v_add_u32_e32 v161, 0x18000, v160
	v_add_u32_e32 v163, 0x18000, v162
	v_add_u32_e32 v165, 0x18000, v164
	v_mov_b32_e32 v82, 0
	v_mov_b32_e32 v83, 0
	v_mov_b32_e32 v84, 0
	v_mov_b32_e32 v85, 0
	v_mov_b32_e32 v58, 0
	v_mov_b32_e32 v59, 0
	v_mov_b32_e32 v60, 0
	v_mov_b32_e32 v61, 0
	v_mov_b32_e32 v14, 0
	v_mov_b32_e32 v15, 0
	v_mov_b32_e32 v16, 0
	v_mov_b32_e32 v17, 0
	v_mov_b32_e32 v78, 0
	v_mov_b32_e32 v79, 0
	v_mov_b32_e32 v80, 0
	v_mov_b32_e32 v81, 0
	v_mov_b32_e32 v22, 0
	v_mov_b32_e32 v23, 0
	v_mov_b32_e32 v24, 0
	v_mov_b32_e32 v25, 0
	v_mov_b32_e32 v30, 0
	v_mov_b32_e32 v31, 0
	v_mov_b32_e32 v32, 0
	v_mov_b32_e32 v33, 0
	v_mov_b32_e32 v74, 0
	v_mov_b32_e32 v75, 0
	v_mov_b32_e32 v76, 0
	v_mov_b32_e32 v77, 0
	v_mov_b32_e32 v18, 0
	v_mov_b32_e32 v19, 0
	v_mov_b32_e32 v20, 0
	v_mov_b32_e32 v21, 0
	v_mov_b32_e32 v26, 0
	v_mov_b32_e32 v27, 0
	v_mov_b32_e32 v28, 0
	v_mov_b32_e32 v29, 0
	v_mov_b32_e32 v70, 0
	v_mov_b32_e32 v71, 0
	v_mov_b32_e32 v72, 0
	v_mov_b32_e32 v73, 0
	v_mov_b32_e32 v46, 0
	v_mov_b32_e32 v47, 0
	v_mov_b32_e32 v48, 0
	v_mov_b32_e32 v49, 0
	v_mov_b32_e32 v240, 0
	v_mov_b32_e32 v241, 0
	v_mov_b32_e32 v242, 0
	v_mov_b32_e32 v243, 0
	v_mov_b32_e32 v66, 0
	v_mov_b32_e32 v67, 0
	v_mov_b32_e32 v68, 0
	v_mov_b32_e32 v69, 0
	v_mov_b32_e32 v42, 0
	v_mov_b32_e32 v43, 0
	v_mov_b32_e32 v44, 0
	v_mov_b32_e32 v45, 0
	v_mov_b32_e32 v236, 0
	v_mov_b32_e32 v237, 0
	v_mov_b32_e32 v238, 0
	v_mov_b32_e32 v239, 0
	v_mov_b32_e32 v62, 0
	v_mov_b32_e32 v63, 0
	v_mov_b32_e32 v64, 0
	v_mov_b32_e32 v65, 0
	v_mov_b32_e32 v38, 0
	v_mov_b32_e32 v39, 0
	v_mov_b32_e32 v40, 0
	v_mov_b32_e32 v41, 0
	v_mov_b32_e32 v34, 0
	v_mov_b32_e32 v35, 0
	v_mov_b32_e32 v36, 0
	v_mov_b32_e32 v37, 0
	s_not_b64 s[6:7], s[4:5]
	s_mov_b32 s22, 4
	s_waitcnt vmcnt(9) lgkmcnt(0)
	s_barrier
	ds_read_b128 v[134:137], v162
	ds_read_b128 v[138:141], v162 offset:2048
	ds_read_b128 v[142:145], v162 offset:4096
	ds_read_b128 v[86:89], v158
	ds_read_b128 v[90:93], v158 offset:2048
	ds_read_b128 v[94:97], v158 offset:4096
	ds_read_b128 v[98:101], v158 offset:6144
	ds_read_b128 v[102:105], v158 offset:8192
	ds_read_b128 v[106:109], v158 offset:10240
	s_cmp_eq_u32 s14, 0
	s_cbranch_scc1 .Lgemm_prio_skip
	s_setprio 1
.Lgemm_prio_skip:
	s_and_b64 vcc, exec, s[4:5]
	s_cbranch_vccnz .Lgemm_N_loop

.LBB1_76:
	s_setprio 0
	v_cmp_gt_u32_e64 s[4:5], 9, v0
	s_waitcnt lgkmcnt(0)
	s_barrier
	s_and_saveexec_b64 s[8:9], s[4:5]
	v_lshlrev_b32_e32 v50, 2, v0
	v_mov_b32_e32 v51, 0
	ds_write_b32 v50, v51
	s_or_b64 exec, exec, s[8:9]
	s_load_dwordx2 s[8:9], s[0:1], 0x28
	s_mul_i32 s11, s14, 0x60
	s_mov_b64 s[12:13], -1
	s_and_b64 vcc, exec, s[6:7]
	v_lshlrev_b32_e32 v87, 3, v231
	s_cbranch_vccnz .LBB1_152
	v_lshlrev_b32_e32 v51, 1, v231
	s_lshr_b32 s6, s2, 6
	v_and_b32_e32 v51, 4, v51
	s_mulk_i32 s6, 0x6c00
	s_addk_i32 s6, 0x400
	v_lshlrev_b32_e32 v90, 1, v51
	s_waitcnt vmcnt(0)
	v_add_f32_e32 v51, v234, v82
	v_and_b32_e32 v50, 8, v87
	v_and_or_b32 v86, s2, 48, v1
	s_movk_i32 s7, 0x190
	v_mov_b32_e32 v52, s6
	v_cvt_f16_f32_e32 v91, v51
	s_cmpk_gt_u32 s17, 0x7ff
	v_mad_u32_u24 v88, v86, s7, v52
	v_lshlrev_b32_e32 v89, 1, v50
	s_cselect_b64 s[12:13], -1, 0
	v_add3_u32 v50, v88, v89, v90
	v_lshlrev_b32_e32 v95, 2, v231
	s_movk_i32 s14, 0xfe72
	s_mov_b64 s[6:7], -1
	s_and_b64 vcc, exec, s[12:13]
	v_add_f32_e32 v92, v234, v85
	v_lshl_add_u32 v96, s11, 1, v50
	s_cbranch_vccz .LBB1_81
	v_cvt_f16_f32_e32 v52, v92
	v_mov_b32_e32 v50, v83
	v_mov_b32_e32 v51, v84
	v_pk_add_f32 v[50:51], v[234:235], v[50:51] op_sel_hi:[0,1]
	v_cvt_pk_f16_f32 v51, v50, v51
	s_mov_b32 s6, 0x5040100
	v_perm_b32 v50, v51, v91, s6
	v_alignbit_b32 v51, v52, v51, 16
	ds_write_b64 v96, v[50:51]
	s_mov_b64 s[6:7], 0
